# step-3 epilogue: eight norm-weight loads issued together; hyena ctx prologue: first filter-value loads merged into the common load batch
# baseline (speedup 1.0000x reference)
.LBB0_733:
	s_ashr_i32 s39, s38, 31
	s_lshl_b64 s[0:1], s[38:39], 11
	s_add_u32 s10, s48, s0
	v_mov_b32_e32 v4, v0
	s_addc_u32 s11, s49, s1
	s_add_u32 s0, s52, s0
	v_ashrrev_i32_e32 v5, 31, v4
	v_lshlrev_b64 v[6:7], 2, v[4:5]
	s_addc_u32 s1, s53, s1
	v_lshl_add_u64 v[8:9], s[10:11], 0, v[6:7]
	v_lshl_add_u64 v[6:7], s[0:1], 0, v[6:7]
	global_load_dword v33, v[8:9], off
	global_load_dword v34, v[6:7], off
	v_lshrrev_b32_e32 v2, 2, v4
	v_add_u32_e32 v2, v2, v4
	s_lshl_b64 s[40:41], s[38:39], 2
	v_lshl_add_u32 v2, v2, 2, 0
	v_mov_b32_e32 v35, v2
	s_add_u32 s0, s46, s40
	s_addc_u32 s1, s47, s41
	v_readlane_b32 s56, v248, 43
	v_readlane_b32 s64, v248, 51
	v_readlane_b32 s65, v248, 52
	v_readlane_b32 s66, v248, 53
	v_readlane_b32 s67, v248, 54
	v_readlane_b32 s68, v248, 55
	v_readlane_b32 s69, v248, 56
	v_readlane_b32 s70, v248, 57
	v_readlane_b32 s71, v248, 58
	s_mov_b64 s[20:21], s[64:65]
	v_readlane_b32 s57, v248, 44
	v_readlane_b32 s58, v248, 45
	v_readlane_b32 s59, v248, 46
	v_readlane_b32 s60, v248, 47
	v_readlane_b32 s61, v248, 48
	v_readlane_b32 s62, v248, 49
	v_readlane_b32 s63, v248, 50
	v_readlane_b32 s56, v248, 0
	v_readlane_b32 s57, v248, 1
	v_readlane_b32 s58, v248, 2
	v_readlane_b32 s59, v248, 3
	v_readlane_b32 s60, v248, 4
	v_readlane_b32 s61, v248, 5
	v_readlane_b32 s62, v248, 6
	v_readlane_b32 s63, v248, 7
	s_mov_b64 s[56:57], s[60:61]
	s_mov_b64 s[58:59], s[62:63]
	v_and_b32_e32 v6, 0xffffff00, v4
	v_ashrrev_i32_e32 v7, 31, v6
	v_and_b32_e32 v12, 0xff, v4
	v_cmp_ne_u32_e32 vcc, 0, v12
	v_mov_b32_e32 v19, 0
	v_mov_b32_e32 v15, 0
	s_mov_b64 s[22:23], s[66:67]
	s_mov_b64 s[24:25], s[68:69]
	s_mov_b64 s[26:27], s[70:71]
	global_load_dword v1, v3, s[0:1]
	global_load_dword v10, v3, s[0:1] offset:2048
	s_add_i32 s0, s38, s12
	s_ashr_i32 s1, s0, 31
	s_lshl_b64 s[0:1], s[0:1], 2
	s_add_u32 s0, s20, s0
	s_addc_u32 s1, s21, s1
	global_load_dword v5, v3, s[0:1]
	s_add_i32 s0, s38, s54
	s_ashr_i32 s1, s0, 31
	s_lshl_b64 s[0:1], s[0:1], 2
	s_add_u32 s0, s20, s0
	s_addc_u32 s1, s21, s1
	global_load_dword v11, v3, s[0:1]
	s_add_i32 s0, s38, 0x80
	s_mul_hi_i32 s1, s0, 0x4400
	s_mulk_i32 s0, 0x4400
	s_add_u32 s0, s58, s0
	s_addc_u32 s1, s59, s1
	v_lshl_add_u64 v[8:9], v[6:7], 1, s[0:1]
	s_mov_b64 s[20:21], 0x41c94000
	v_lshl_add_u64 v[8:9], v[8:9], 0, s[20:21]
	v_lshlrev_b32_e32 v2, 1, v12
	s_and_saveexec_b64 s[0:1], vcc
	s_cbranch_execz .LBB0_735
	v_lshl_add_u64 v[14:15], v[8:9], 0, v[2:3]
	global_load_ushort v15, v[14:15], off offset:-2

.LBB0_745:
	s_or_b64 exec, exec, s[10:11]
	v_mov_b32_e32 v8, 0x4000
	global_load_dword v26, v218, s[40:41] offset:2048
	global_load_dword v27, v8, s[40:41]
	v_mov_b32_e32 v8, 0x1000
	global_load_dword v28, v8, s[40:41]
	s_waitcnt vmcnt(3)
	ds_write2st64_b32 v35, v33, v34 offset1:10
	v_lshlrev_b32_e32 v15, 16, v15
	v_lshlrev_b32_e32 v19, 16, v19
	v_lshlrev_b32_e32 v17, 16, v17
	v_lshlrev_b32_e32 v21, 16, v21
	v_lshlrev_b32_e32 v23, 16, v23
	v_lshlrev_b32_e32 v7, 16, v7
	v_lshlrev_b32_e32 v29, 16, v2
	v_lshlrev_b32_e32 v2, 16, v25
	v_lshlrev_b32_e32 v9, 16, v14
	v_mul_f32_e32 v2, v24, v2
	s_mul_i32 s0, s38, 0x4400
	v_lshlrev_b32_e32 v14, 2, v4
	v_add3_u32 v8, v6, v12, s84
	v_mul_f32_e32 v6, v13, v9
	v_readlane_b32 s10, v251, 44
	v_fmac_f32_e32 v2, v17, v18
	s_mul_hi_i32 s1, s38, 0x4400
	v_ashrrev_i32_e32 v25, 7, v4
	v_lshlrev_b32_e32 v30, 4, v4
	v_and_b32_e32 v4, 63, v4
	v_readlane_b32 s11, v251, 45
	s_add_u32 s0, s10, s0
	v_and_b32_e32 v13, 0x100, v14
	v_fmac_f32_e32 v6, v15, v16
	v_fmac_f32_e32 v2, v21, v22
	v_add_u32_e32 v12, 0, v14
	v_lshlrev_b32_e32 v24, 6, v25
	v_lshl_add_u32 v31, v25, 11, 0
	v_and_b32_e32 v30, 0x3f0, v30
	v_ashrrev_i32_e32 v9, 31, v8
	v_lshlrev_b32_e32 v32, 2, v4
	v_lshlrev_b32_e32 v14, 8, v25
	v_lshlrev_b32_e32 v4, 4, v4
	s_addc_u32 s1, s11, s1
	v_lshlrev_b32_e32 v25, 2, v13
	v_fmac_f32_e32 v6, v19, v20
	v_or_b32_e32 v15, 48, v24
	v_add_u32_e32 v16, -16, v24
	v_sub_u32_e32 v17, 0, v32
	v_sub_u32_e32 v18, 0, v4
	v_add3_u32 v19, v31, v25, v30
	v_lshl_add_u64 v[8:9], v[8:9], 1, s[0:1]
	v_mul_f32_e32 v20, v5, v6
	s_mov_b64 s[40:41], -1
	ds_write2st64_b32 v12, v6, v2 offset0:20 offset1:28
	s_waitcnt vmcnt(2)
	v_mul_f32_e32 v21, v26, v29
	s_waitcnt vmcnt(0)
	v_fmac_f32_e32 v21, v23, v28
	v_fmac_f32_e32 v21, v7, v27
	ds_write_b32 v12, v21 offset:9216
	s_branch .LBB0_747

.LBB0_1145:
	s_or_b64 exec, exec, s[0:1]
	s_lshl_b32 s0, s40, 2
	s_add_u32 s0, s10, s0
	v_or_b32_e32 v28, s56, v228
	s_addc_u32 s1, s11, 0
	v_ashrrev_i32_e32 v29, 31, v28
	v_lshl_add_u64 v[8:9], v[28:29], 2, s[0:1]
	s_waitcnt lgkmcnt(0)
	s_barrier
	global_load_dwordx4 v[24:27], v[8:9], off
	global_load_dwordx4 v[36:39], v[8:9], off offset:32
	global_load_dwordx4 v[40:43], v[8:9], off offset:64
	global_load_dwordx4 v[44:47], v[8:9], off offset:96
	global_load_dwordx4 v[48:51], v[8:9], off offset:128
	global_load_dwordx4 v[52:55], v[8:9], off offset:160
	global_load_dwordx4 v[56:59], v[8:9], off offset:192
	global_load_dwordx4 v[60:63], v[8:9], off offset:224
	v_lshl_add_u32 v1, v227, 2, 0
	s_waitcnt vmcnt(11)
	v_lshlrev_b32_e32 v2, 16, v22
	v_and_b32_e32 v22, 0xffff0000, v22
	v_lshlrev_b32_e32 v30, 16, v23
	v_and_b32_e32 v23, 0xffff0000, v23
	v_add_u32_e32 v1, 0x1b000, v1
	v_ashrrev_i32_e32 v21, 31, v20
	v_mul_f32_e32 v2, 0xbfb8aa3b, v2
	v_mul_f32_e32 v31, 0xbfb8aa3b, v22
	v_mul_f32_e32 v32, 0xbfb8aa3b, v23
	ds_read2st64_b32 v[22:23], v1 offset1:2
	v_readlane_b32 s36, v248, 0
	v_lshlrev_b64 v[20:21], 12, v[20:21]
	v_readlane_b32 s42, v248, 6
	v_readlane_b32 s43, v248, 7
	v_exp_f32_e32 v1, v2
	s_mov_b32 s0, 0x43830000
	v_lshl_add_u64 v[20:21], s[42:43], 0, v[20:21]
	v_lshl_add_u64 v[20:21], v[20:21], 0, s[12:13]
	v_lshl_add_u64 v[28:29], v[28:29], 1, v[20:21]
	v_add_co_u32_e32 v20, vcc, s0, v28
	v_add_f32_e32 v1, 1.0, v1
	s_waitcnt lgkmcnt(0)
	v_add_f32_e32 v23, v22, v23
	v_addc_co_u32_e32 v21, vcc, 0, v29, vcc
	v_rcp_f32_e32 v22, v1
	v_fmamk_f32 v1, v23, 0x3c000000, v213
	s_mov_b32 s0, 0x800000
	v_mul_f32_e32 v30, 0xbfb8aa3b, v30
	v_mul_f32_e32 v23, 0x4b800000, v1
	v_cmp_gt_f32_e32 vcc, s0, v1
	v_exp_f32_e32 v2, v31
	v_exp_f32_e32 v30, v30
	v_exp_f32_e32 v31, v32
	v_cndmask_b32_e32 v1, v1, v23, vcc
	v_rsq_f32_e32 v1, v1
	v_add_f32_e32 v2, 1.0, v2
	v_add_f32_e32 v30, 1.0, v30
	v_add_f32_e32 v31, 1.0, v31
	v_rcp_f32_e32 v23, v2
	v_rcp_f32_e32 v30, v30
	v_rcp_f32_e32 v31, v31
	v_mul_f32_e32 v2, 0x45800000, v1
	v_cndmask_b32_e32 v2, v1, v2, vcc
	v_pk_mul_f32 v[32:33], v[184:185], v[2:3] op_sel_hi:[1,0]
	v_pk_mul_f32 v[34:35], v[186:187], v[2:3] op_sel_hi:[1,0]
	v_lshlrev_b32_e32 v1, 16, v12
	v_and_b32_e32 v12, 0xffff0000, v12
	v_mul_f32_e32 v1, 0xbfb8aa3b, v1
	v_mul_f32_e32 v12, 0xbfb8aa3b, v12
	v_exp_f32_e32 v1, v1
	s_mov_b64 s[0:1], 0x43830800
	v_readlane_b32 s37, v248, 1
	v_readlane_b32 s38, v248, 2
	v_add_f32_e32 v1, 1.0, v1
	v_readlane_b32 s39, v248, 3
	v_readlane_b32 s40, v248, 4
	v_readlane_b32 s41, v248, 5
	s_waitcnt vmcnt(7)
	v_pk_mul_f32 v[24:25], v[24:25], v[32:33]
	v_pk_mul_f32 v[26:27], v[26:27], v[34:35]
	v_pk_mul_f32 v[22:23], v[22:23], v[24:25]
	v_pk_mul_f32 v[24:25], v[30:31], v[26:27]
	v_cvt_pk_bf16_f32 v22, v22, v23
	v_cvt_pk_bf16_f32 v23, v24, v25
	global_store_dwordx2 v[20:21], v[22:23], off offset:2048
	v_lshlrev_b32_e32 v24, 16, v13
	v_and_b32_e32 v13, 0xffff0000, v13
	v_mul_f32_e32 v24, 0xbfb8aa3b, v24
	v_mul_f32_e32 v13, 0xbfb8aa3b, v13
	v_exp_f32_e32 v25, v12
	v_exp_f32_e32 v24, v24
	v_exp_f32_e32 v26, v13
	v_lshl_add_u64 v[12:13], v[28:29], 0, s[0:1]
	v_add_f32_e32 v25, 1.0, v25
	v_add_f32_e32 v27, 1.0, v24
	v_add_f32_e32 v28, 1.0, v26
	v_rcp_f32_e32 v24, v1
	v_rcp_f32_e32 v25, v25
	v_rcp_f32_e32 v26, v27
	v_rcp_f32_e32 v27, v28
	v_pk_mul_f32 v[28:29], v[182:183], v[2:3] op_sel_hi:[1,0]
	v_pk_mul_f32 v[30:31], v[172:173], v[2:3] op_sel_hi:[1,0]
	v_lshlrev_b32_e32 v1, 16, v18
	v_and_b32_e32 v18, 0xffff0000, v18
	v_mul_f32_e32 v1, 0xbfb8aa3b, v1
	v_mul_f32_e32 v18, 0xbfb8aa3b, v18
	v_exp_f32_e32 v1, v1
	v_exp_f32_e32 v18, v18
	v_add_f32_e32 v1, 1.0, v1
	s_waitcnt vmcnt(7)
	v_pk_mul_f32 v[20:21], v[36:37], v[28:29]
	v_pk_mul_f32 v[22:23], v[38:39], v[30:31]
	v_pk_mul_f32 v[20:21], v[24:25], v[20:21]
	v_pk_mul_f32 v[22:23], v[26:27], v[22:23]
	v_cvt_pk_bf16_f32 v20, v20, v21
	v_cvt_pk_bf16_f32 v21, v22, v23
	global_store_dwordx2 v[12:13], v[20:21], off offset:16
	v_lshlrev_b32_e32 v24, 16, v19
	v_and_b32_e32 v19, 0xffff0000, v19
	v_mul_f32_e32 v24, 0xbfb8aa3b, v24
	v_mul_f32_e32 v19, 0xbfb8aa3b, v19
	v_exp_f32_e32 v24, v24
	v_exp_f32_e32 v19, v19
	v_add_f32_e32 v25, 1.0, v18
	v_rcp_f32_e32 v18, v1
	v_add_f32_e32 v24, 1.0, v24
	v_add_f32_e32 v26, 1.0, v19
	v_rcp_f32_e32 v19, v25
	v_rcp_f32_e32 v24, v24
	v_rcp_f32_e32 v25, v26
	v_pk_mul_f32 v[26:27], v[170:171], v[2:3] op_sel_hi:[1,0]
	v_pk_mul_f32 v[28:29], v[168:169], v[2:3] op_sel_hi:[1,0]
	v_lshlrev_b32_e32 v1, 16, v16
	v_and_b32_e32 v16, 0xffff0000, v16
	v_mul_f32_e32 v1, 0xbfb8aa3b, v1
	v_mul_f32_e32 v16, 0xbfb8aa3b, v16
	v_exp_f32_e32 v1, v1
	v_exp_f32_e32 v16, v16
	v_add_f32_e32 v1, 1.0, v1
	s_waitcnt vmcnt(7)
	v_pk_mul_f32 v[20:21], v[26:27], v[40:41]
	v_pk_mul_f32 v[22:23], v[28:29], v[42:43]
	v_pk_mul_f32 v[18:19], v[18:19], v[20:21]
	v_pk_mul_f32 v[20:21], v[24:25], v[22:23]
	v_cvt_pk_bf16_f32 v18, v18, v19
	v_cvt_pk_bf16_f32 v19, v20, v21
	global_store_dwordx2 v[12:13], v[18:19], off offset:32
	v_lshlrev_b32_e32 v22, 16, v17
	v_and_b32_e32 v17, 0xffff0000, v17
	v_mul_f32_e32 v22, 0xbfb8aa3b, v22
	v_mul_f32_e32 v17, 0xbfb8aa3b, v17
	v_exp_f32_e32 v22, v22
	v_exp_f32_e32 v17, v17
	v_add_f32_e32 v23, 1.0, v16
	v_rcp_f32_e32 v16, v1
	v_add_f32_e32 v22, 1.0, v22
	v_add_f32_e32 v24, 1.0, v17
	v_rcp_f32_e32 v17, v23
	v_rcp_f32_e32 v22, v22
	v_rcp_f32_e32 v23, v24
	v_pk_mul_f32 v[24:25], v[166:167], v[2:3] op_sel_hi:[1,0]
	v_pk_mul_f32 v[26:27], v[164:165], v[2:3] op_sel_hi:[1,0]
	v_lshlrev_b32_e32 v1, 16, v14
	v_and_b32_e32 v14, 0xffff0000, v14
	v_mul_f32_e32 v1, 0xbfb8aa3b, v1
	v_mul_f32_e32 v14, 0xbfb8aa3b, v14
	v_exp_f32_e32 v1, v1
	v_exp_f32_e32 v14, v14
	v_add_f32_e32 v1, 1.0, v1
	s_waitcnt vmcnt(7)
	v_pk_mul_f32 v[18:19], v[24:25], v[44:45]
	v_pk_mul_f32 v[20:21], v[26:27], v[46:47]
	v_pk_mul_f32 v[16:17], v[16:17], v[18:19]
	v_pk_mul_f32 v[18:19], v[22:23], v[20:21]
	v_cvt_pk_bf16_f32 v16, v16, v17
	v_cvt_pk_bf16_f32 v17, v18, v19
	global_store_dwordx2 v[12:13], v[16:17], off offset:48
	v_lshlrev_b32_e32 v20, 16, v15
	v_and_b32_e32 v15, 0xffff0000, v15
	v_mul_f32_e32 v20, 0xbfb8aa3b, v20
	v_mul_f32_e32 v15, 0xbfb8aa3b, v15
	v_exp_f32_e32 v20, v20
	v_exp_f32_e32 v15, v15
	v_add_f32_e32 v21, 1.0, v14
	v_rcp_f32_e32 v14, v1
	v_add_f32_e32 v20, 1.0, v20
	v_add_f32_e32 v22, 1.0, v15
	v_rcp_f32_e32 v15, v21
	v_rcp_f32_e32 v20, v20
	v_rcp_f32_e32 v21, v22
	v_pk_mul_f32 v[22:23], v[162:163], v[2:3] op_sel_hi:[1,0]
	v_pk_mul_f32 v[24:25], v[160:161], v[2:3] op_sel_hi:[1,0]
	v_lshlrev_b32_e32 v1, 16, v10
	v_and_b32_e32 v10, 0xffff0000, v10
	v_mul_f32_e32 v1, 0xbfb8aa3b, v1
	v_mul_f32_e32 v10, 0xbfb8aa3b, v10
	v_exp_f32_e32 v1, v1
	v_exp_f32_e32 v10, v10
	v_add_f32_e32 v1, 1.0, v1
	s_waitcnt vmcnt(7)
	v_pk_mul_f32 v[16:17], v[22:23], v[48:49]
	v_pk_mul_f32 v[18:19], v[24:25], v[50:51]
	v_pk_mul_f32 v[14:15], v[14:15], v[16:17]
	v_pk_mul_f32 v[16:17], v[20:21], v[18:19]
	v_cvt_pk_bf16_f32 v14, v14, v15
	v_cvt_pk_bf16_f32 v15, v16, v17
	global_store_dwordx2 v[12:13], v[14:15], off offset:64
	v_lshlrev_b32_e32 v18, 16, v11
	v_and_b32_e32 v11, 0xffff0000, v11
	v_mul_f32_e32 v18, 0xbfb8aa3b, v18
	v_mul_f32_e32 v11, 0xbfb8aa3b, v11
	v_exp_f32_e32 v18, v18
	v_exp_f32_e32 v11, v11
	v_add_f32_e32 v19, 1.0, v10
	v_rcp_f32_e32 v10, v1
	v_add_f32_e32 v18, 1.0, v18
	v_add_f32_e32 v20, 1.0, v11
	v_rcp_f32_e32 v11, v19
	v_rcp_f32_e32 v18, v18
	v_rcp_f32_e32 v19, v20
	v_pk_mul_f32 v[20:21], v[158:159], v[2:3] op_sel_hi:[1,0]
	v_pk_mul_f32 v[22:23], v[156:157], v[2:3] op_sel_hi:[1,0]
	v_lshlrev_b32_e32 v1, 16, v6
	v_and_b32_e32 v6, 0xffff0000, v6
	v_mul_f32_e32 v1, 0xbfb8aa3b, v1
	v_mul_f32_e32 v6, 0xbfb8aa3b, v6
	v_exp_f32_e32 v1, v1
	v_exp_f32_e32 v6, v6
	v_add_f32_e32 v1, 1.0, v1
	s_waitcnt vmcnt(7)
	v_pk_mul_f32 v[14:15], v[20:21], v[52:53]
	v_pk_mul_f32 v[16:17], v[22:23], v[54:55]
	v_pk_mul_f32 v[10:11], v[10:11], v[14:15]
	v_pk_mul_f32 v[14:15], v[18:19], v[16:17]
	v_cvt_pk_bf16_f32 v10, v10, v11
	v_cvt_pk_bf16_f32 v11, v14, v15
	global_store_dwordx2 v[12:13], v[10:11], off offset:80
	v_lshlrev_b32_e32 v10, 16, v7
	v_and_b32_e32 v7, 0xffff0000, v7
	v_mul_f32_e32 v10, 0xbfb8aa3b, v10
	v_mul_f32_e32 v7, 0xbfb8aa3b, v7
	v_exp_f32_e32 v10, v10
	v_exp_f32_e32 v7, v7
	v_add_f32_e32 v11, 1.0, v6
	v_rcp_f32_e32 v6, v1
	v_add_f32_e32 v10, 1.0, v10
	v_add_f32_e32 v18, 1.0, v7
	v_rcp_f32_e32 v7, v11
	v_rcp_f32_e32 v10, v10
	v_rcp_f32_e32 v11, v18
	v_pk_mul_f32 v[18:19], v[154:155], v[2:3] op_sel_hi:[1,0]
	v_pk_mul_f32 v[20:21], v[152:153], v[2:3] op_sel_hi:[1,0]
	v_lshlrev_b32_e32 v1, 16, v4
	v_and_b32_e32 v4, 0xffff0000, v4
	v_mul_f32_e32 v1, 0xbfb8aa3b, v1
	v_mul_f32_e32 v4, 0xbfb8aa3b, v4
	v_exp_f32_e32 v1, v1
	v_exp_f32_e32 v4, v4
	v_add_f32_e32 v1, 1.0, v1
	s_waitcnt vmcnt(7)
	v_pk_mul_f32 v[14:15], v[18:19], v[56:57]
	v_pk_mul_f32 v[16:17], v[20:21], v[58:59]
	v_pk_mul_f32 v[6:7], v[6:7], v[14:15]
	v_pk_mul_f32 v[10:11], v[10:11], v[16:17]
	v_cvt_pk_bf16_f32 v6, v6, v7
	v_cvt_pk_bf16_f32 v7, v10, v11
	global_store_dwordx2 v[12:13], v[6:7], off offset:96
	v_lshlrev_b32_e32 v10, 16, v5
	v_and_b32_e32 v5, 0xffff0000, v5
	v_mul_f32_e32 v10, 0xbfb8aa3b, v10
	v_mul_f32_e32 v5, 0xbfb8aa3b, v5
	v_exp_f32_e32 v10, v10
	v_exp_f32_e32 v5, v5
	v_add_f32_e32 v11, 1.0, v4
	v_rcp_f32_e32 v4, v1
	v_add_f32_e32 v10, 1.0, v10
	v_add_f32_e32 v14, 1.0, v5
	v_rcp_f32_e32 v5, v11
	v_rcp_f32_e32 v10, v10
	v_rcp_f32_e32 v11, v14
	v_pk_mul_f32 v[14:15], v[150:151], v[2:3] op_sel_hi:[1,0]
	v_pk_mul_f32 v[16:17], v[148:149], v[2:3] op_sel_hi:[1,0]
	s_waitcnt vmcnt(7)
	v_pk_mul_f32 v[6:7], v[14:15], v[60:61]
	v_pk_mul_f32 v[8:9], v[16:17], v[62:63]
	v_pk_mul_f32 v[4:5], v[4:5], v[6:7]
	v_pk_mul_f32 v[6:7], v[10:11], v[8:9]
	v_cvt_pk_bf16_f32 v4, v4, v5
	v_cvt_pk_bf16_f32 v5, v6, v7
	global_store_dwordx2 v[12:13], v[4:5], off offset:112
	s_barrier
